# baseline (speedup 1.0000x reference)
_Z8k_layer2PKhPKfPK15HIP_vector_typeIjLj4EEPKjS2_PKDF16_S2_Pf:
	s_mov_b64 s[30:31], s[0:1]
	s_mov_b32 s32, s2
	s_mov_b32 s33, 1
	v_mov_b32_e32 v112, v0
.Lrep_l2:
	s_lshl_b32 s3, s2, 2
	s_and_b32 s3, s3, 28
	s_and_b32 s12, s2, 0xffffffe0
	s_or_b32 s3, s3, s12
	s_bfe_u32 s12, s2, 0x20003
	s_or_b32 s3, s3, s12
	s_load_dwordx8 s[4:11], s[0:1], 0x0
	s_cmpk_eq_i32 s2, 0x3ef
	s_movk_i32 s12, 0x3f7
	s_cselect_b32 s12, s12, 0x3fb
	s_cmpk_gt_i32 s3, 0x3fc
	s_cselect_b32 s12, s12, s3
	v_lshrrev_b32_e32 v80, 3, v0
	v_lshl_or_b32 v6, s12, 5, v80
	v_ashrrev_i32_e32 v7, 31, v6
	v_or_b32_e32 v83, 0x200, v0
	v_or_b32_e32 v82, 0x300, v0
	s_waitcnt lgkmcnt(0)
	v_lshl_add_u64 v[2:3], v[6:7], 4, s[8:9]
	v_lshlrev_b32_e32 v14, 2, v0
	v_or_b32_e32 v84, 0x100, v0
	v_lshlrev_b32_e32 v7, 2, v83
	v_min_u32_e32 v8, 0x3fc, v82
	global_load_dwordx4 v[2:5], v[2:3], off
	v_lshlrev_b32_e32 v1, 2, v84
	v_lshlrev_b32_e32 v8, 2, v8
	global_load_dword v15, v14, s[6:7]
	global_load_dword v16, v1, s[6:7]
	global_load_dword v17, v7, s[6:7]
	global_load_dword v18, v8, s[6:7]
	s_movk_i32 s13, 0x188
	v_mad_u64_u32 v[6:7], s[8:9], s12, 17, v[6:7]
	v_min_i32_e32 v1, 0xc350, v6
	v_mov_b32_e32 v10, 0xc350
	v_cmp_gt_u32_e32 vcc, s13, v0
	v_lshlrev_b32_e32 v81, 4, v0
	v_and_b32_e32 v60, 0x70, v81
	v_cndmask_b32_e32 v6, v10, v1, vcc
	v_mov_b32_e32 v61, 0
	v_ashrrev_i32_e32 v7, 31, v6
	s_mul_i32 s3, s12, 49
	v_lshl_add_u64 v[8:9], s[4:5], 0, v[60:61]
	v_lshlrev_b64 v[6:7], 7, v[6:7]
	v_lshrrev_b32_e32 v1, 3, v84
	v_lshl_add_u64 v[38:39], v[8:9], 0, v[6:7]
	s_movk_i32 s8, 0x88
	v_add_u32_e32 v6, s3, v1
	v_min_i32_e32 v6, 0xc350, v6
	v_cmp_gt_u32_e32 vcc, s8, v0
	s_ashr_i32 s13, s12, 31
	s_lshl_b64 s[8:9], s[12:13], 2
	v_cndmask_b32_e32 v6, v10, v6, vcc
	v_ashrrev_i32_e32 v7, 31, v6
	v_lshlrev_b64 v[6:7], 7, v[6:7]
	v_lshl_add_u64 v[40:41], v[8:9], 0, v[6:7]
	global_load_dwordx4 v[10:13], v[38:39], off
	global_load_dwordx4 v[6:9], v[40:41], off
	s_add_u32 s8, s6, s8
	s_addc_u32 s9, s7, s9
	s_load_dword s18, s[8:9], 0x0
	s_load_dwordx4 s[12:15], s[0:1], 0x28
	s_load_dwordx2 s[6:7], s[0:1], 0x38
	v_cmp_gt_u32_e32 vcc, 64, v0
	s_waitcnt vmcnt(4)
	ds_write2st64_b32 v14, v15, v16 offset0:136 offset1:140
	v_and_b32_e32 v105, 7, v0
	v_sub_co_u32_e64 v106, s[22:23], v105, v3
	v_add_u32_e32 v107, v2, v105
	v_add_u32_e32 v106, v106, v4
	v_cndmask_b32_e64 v106, v106, v107, s[22:23]
	v_mov_b32_e32 v107, 0
	v_lshl_add_u64 v[106:107], v[106:107], 2, s[10:11]
	global_load_dword v104, v[106:107], off
	s_waitcnt vmcnt(3)
	ds_write2st64_b32 v14, v17, v18 offset0:144 offset1:148
	s_and_saveexec_b64 s[8:9], vcc
	s_cbranch_execz .LBB3_4
	v_cmp_gt_u32_e32 vcc, 49, v0
	v_mov_b32_e32 v15, 1.0
	s_and_saveexec_b64 s[16:17], vcc
	s_cbranch_execz .LBB3_3
	s_load_dwordx2 s[0:1], s[0:1], 0x20
	v_add_u32_e32 v15, s3, v0
	v_min_i32_e32 v16, 0xc34f, v15
	v_ashrrev_i32_e32 v17, 31, v16
	s_waitcnt lgkmcnt(0)
	v_lshl_add_u64 v[16:17], v[16:17], 2, s[0:1]
	global_load_dword v16, v[16:17], off
	s_mov_b32 s0, 0xc350
	v_cmp_gt_i32_e32 vcc, s0, v15
	s_waitcnt vmcnt(0)
	s_nop 0
	v_cndmask_b32_e32 v15, 1.0, v16, vcc

.LBB3_26:
	s_or_b64 exec, exec, s[0:1]
	s_cmp_eq_u32 s33, 1
	s_cbranch_scc1 .Lpass_end_l2
	v_and_b32_e32 v62, 63, v0
	v_bfe_u32 v63, v0, 5, 1
	v_lshrrev_b32_e32 v64, 6, v0
	v_and_b32_e32 v65, 31, v0
	s_setprio 0
	s_waitcnt vmcnt(1)
	v_lshlrev_b32_e32 v10, 4, v62
	v_lshl_or_b32 v10, v64, 13, v10
	v_mov_b32_e32 v11, 0
	v_lshl_add_u64 v[12:13], s[12:13], 0, v[10:11]
	s_movk_i32 s0, 0x1000
	s_waitcnt lgkmcnt(0)
	global_load_dwordx4 v[6:9], v[38:39], off
	global_load_dwordx4 v[2:5], v[40:41], off
	global_load_dwordx4 v[16:19], v10, s[12:13]
	global_load_dwordx4 v[56:59], v10, s[12:13] offset:1024
	global_load_dwordx4 v[52:55], v10, s[12:13] offset:2048
	global_load_dwordx4 v[48:51], v10, s[12:13] offset:3072
	v_add_co_u32_e32 v10, vcc, s0, v12
	v_lshrrev_b32_e32 v23, 4, v0
	s_nop 0
	v_addc_co_u32_e32 v11, vcc, 0, v13, vcc
	global_load_dwordx4 v[44:47], v[10:11], off
	global_load_dwordx4 v[40:43], v[10:11], off offset:1024
	global_load_dwordx4 v[36:39], v[10:11], off offset:2048
	global_load_dwordx4 v[32:35], v[10:11], off offset:3072
	v_lshlrev_b32_e32 v10, 1, v0
	v_and_b32_e32 v11, 28, v10
	v_lshlrev_b32_e32 v10, 8, v0
	v_and_b32_e32 v21, 0x100, v10
	v_mul_u32_u24_e32 v10, 0x220, v23
	v_or_b32_e32 v10, v11, v10
	v_lshlrev_b32_e32 v0, 2, v23
	v_add_u32_e32 v26, v10, v21
	s_barrier
	ds_read_b32 v0, v0 offset:38912
	ds_read2_b32 v[12:13], v26 offset1:8
	ds_read2_b32 v[14:15], v26 offset0:16 offset1:24
	v_lshrrev_b32_e32 v66, 4, v84
	v_lshrrev_b32_e32 v67, 4, v83
	v_lshrrev_b32_e32 v68, 4, v82
	v_lshlrev_b32_e32 v10, 2, v66
	v_lshlrev_b32_e32 v22, 2, v67
	v_lshlrev_b32_e32 v24, 2, v68
	ds_read_b32 v20, v10 offset:38912
	ds_read_b32 v22, v22 offset:38912
	ds_read_b32 v10, v24 offset:38912
	ds_read2_b32 v[24:25], v26 offset0:32 offset1:40
	s_waitcnt lgkmcnt(5)
	v_fma_mixlo_f16 v69, v0, v12, 0
	v_mov_b32_e32 v12, v13
	s_waitcnt lgkmcnt(4)
	v_mov_b32_e32 v13, v14
	v_mul_f32_e32 v12, v0, v12
	v_mul_f32_e32 v13, v0, v13
	v_cvt_pk_f16_f32 v70, v12, v13
	v_mov_b32_e32 v12, v15
	s_waitcnt lgkmcnt(0)
	v_mov_b32_e32 v13, v24
	v_mul_f32_e32 v12, v0, v12
	v_mul_f32_e32 v13, v0, v13
	v_cvt_pk_f16_f32 v71, v12, v13
	v_mul_u32_u24_e32 v13, 0x220, v66
	ds_read2_b32 v[26:27], v26 offset0:48 offset1:56
	v_or_b32_e32 v13, v11, v13
	v_add_u32_e32 v28, v13, v21
	ds_read2_b32 v[14:15], v28 offset1:8
	v_mov_b32_e32 v12, v25
	s_waitcnt lgkmcnt(1)
	v_mov_b32_e32 v13, v26
	ds_read2_b32 v[24:25], v28 offset0:16 offset1:24
	v_mul_f32_e32 v12, v0, v12
	v_mul_f32_e32 v13, v0, v13
	v_cvt_pk_f16_f32 v26, v12, v13
	s_waitcnt lgkmcnt(1)
	v_fma_mixlo_f16 v72, v20, v14, 0
	v_mov_b32_e32 v12, v15
	ds_read2_b32 v[14:15], v28 offset0:32 offset1:40
	s_waitcnt lgkmcnt(1)
	v_mov_b32_e32 v13, v24
	v_mul_f32_e32 v12, v20, v12
	v_mul_f32_e32 v13, v20, v13
	v_cvt_pk_f16_f32 v73, v12, v13
	v_mov_b32_e32 v12, v25
	s_waitcnt lgkmcnt(0)
	v_mov_b32_e32 v13, v14
	v_mul_f32_e32 v12, v20, v12
	v_mul_f32_e32 v13, v20, v13
	v_cvt_pk_f16_f32 v74, v12, v13
	v_mul_u32_u24_e32 v13, 0x220, v67
	ds_read2_b32 v[24:25], v28 offset0:48 offset1:56
	v_or_b32_e32 v13, v11, v13
	v_add_u32_e32 v30, v13, v21
	v_mov_b32_e32 v12, v15
	ds_read2_b32 v[14:15], v30 offset1:8
	s_waitcnt lgkmcnt(1)
	v_mov_b32_e32 v13, v24
	ds_read2_b32 v[28:29], v30 offset0:16 offset1:24
	v_mul_f32_e32 v12, v20, v12
	v_mul_f32_e32 v13, v20, v13
	v_cvt_pk_f16_f32 v24, v12, v13
	s_waitcnt lgkmcnt(1)
	v_fma_mixlo_f16 v75, v22, v14, 0
	v_mov_b32_e32 v12, v15
	ds_read2_b32 v[14:15], v30 offset0:32 offset1:40
	s_waitcnt lgkmcnt(1)
	v_mov_b32_e32 v13, v28
	v_mul_f32_e32 v12, v22, v12
	v_mul_f32_e32 v13, v22, v13
	v_cvt_pk_f16_f32 v76, v12, v13
	v_mov_b32_e32 v12, v29
	s_waitcnt lgkmcnt(0)
	v_mov_b32_e32 v13, v14
	v_mul_f32_e32 v12, v22, v12
	v_mul_f32_e32 v13, v22, v13
	v_cvt_pk_f16_f32 v77, v12, v13
	v_mul_u32_u24_e32 v13, 0x220, v68
	ds_read2_b32 v[28:29], v30 offset0:48 offset1:56
	v_or_b32_e32 v11, v11, v13
	v_add_u32_e32 v11, v11, v21
	v_mov_b32_e32 v12, v15
	ds_read2_b32 v[14:15], v11 offset1:8
	ds_read2_b32 v[30:31], v11 offset0:16 offset1:24
	s_waitcnt lgkmcnt(2)
	v_mov_b32_e32 v13, v28
	v_mul_f32_e32 v12, v22, v12
	v_mul_f32_e32 v13, v22, v13
	v_cvt_pk_f16_f32 v21, v12, v13
	s_waitcnt lgkmcnt(1)
	v_fma_mixlo_f16 v28, v10, v14, 0
	v_mov_b32_e32 v12, v15
	s_waitcnt lgkmcnt(0)
	v_mov_b32_e32 v13, v30
	ds_read2_b32 v[14:15], v11 offset0:32 offset1:40
	v_mul_f32_e32 v12, v10, v12
	v_mul_f32_e32 v13, v10, v13
	v_cvt_pk_f16_f32 v78, v12, v13
	v_mov_b32_e32 v12, v31
	ds_read2_b32 v[30:31], v11 offset0:48 offset1:56
	s_waitcnt lgkmcnt(1)
	v_mov_b32_e32 v13, v14
	v_mul_f32_e32 v12, v10, v12
	v_mul_f32_e32 v13, v10, v13
	v_cvt_pk_f16_f32 v11, v12, v13
	v_mov_b32_e32 v12, v15
	s_waitcnt lgkmcnt(0)
	v_mov_b32_e32 v13, v30
	v_mul_f32_e32 v12, v10, v12
	v_mul_f32_e32 v13, v10, v13
	v_and_b32_e32 v79, 0xf0, v81
	v_lshrrev_b32_e32 v15, 16, v26
	s_movk_i32 s0, 0x110
	v_cvt_pk_f16_f32 v30, v12, v13
	v_pack_b32_f16 v12, v69, v70
	v_alignbit_b32 v13, v71, v70, 16
	v_alignbit_b32 v14, v26, v71, 16
	v_fma_mixhi_f16 v15, v0, v27, 0
	v_mad_u32_u24 v0, v23, s0, v79
	s_barrier
	ds_write_b128 v0, v[12:15]
	v_lshrrev_b32_e32 v15, 16, v24
	v_pack_b32_f16 v12, v72, v73
	v_alignbit_b32 v13, v74, v73, 16
	v_alignbit_b32 v14, v24, v74, 16
	v_fma_mixhi_f16 v15, v20, v25, 0
	v_mad_u32_u24 v0, v66, s0, v79
	ds_write_b128 v0, v[12:15]
	v_lshrrev_b32_e32 v15, 16, v21
	v_pack_b32_f16 v12, v75, v76
	v_alignbit_b32 v13, v77, v76, 16
	v_alignbit_b32 v14, v21, v77, 16
	v_fma_mixhi_f16 v15, v22, v29, 0
	v_mad_u32_u24 v0, v67, s0, v79
	ds_write_b128 v0, v[12:15]
	v_lshlrev_b32_e32 v0, 2, v80
	ds_read_b32 v0, v0 offset:38912
	v_lshrrev_b32_e32 v15, 16, v30
	v_fma_mixhi_f16 v15, v10, v31, 0
	v_lshlrev_b32_e32 v10, 2, v1
	ds_read_b32 v24, v10 offset:38912
	s_waitcnt lgkmcnt(1)
	v_div_scale_f32 v10, s[4:5], v0, v0, s18
	v_alignbit_b32 v13, v11, v78, 16
	v_alignbit_b32 v14, v30, v11, 16
	v_rcp_f32_e32 v11, v10
	v_pack_b32_f16 v12, v28, v78
	v_mad_u32_u24 v20, v68, s0, v79
	ds_write_b128 v20, v[12:15]
	v_fma_f32 v12, -v10, v11, 1.0
	v_fmac_f32_e32 v11, v12, v11
	v_div_scale_f32 v12, vcc, s18, v0, s18
	v_mul_f32_e32 v13, v12, v11
	v_fma_f32 v14, -v10, v13, v12
	v_fmac_f32_e32 v13, v14, v11
	v_fma_f32 v10, -v10, v13, v12
	v_div_fmas_f32 v10, v10, v11, v13
	v_div_fixup_f32 v0, v10, v0, s18
	s_waitcnt vmcnt(9)
	v_cvt_f32_ubyte1_e32 v13, v8
	v_cvt_f32_ubyte0_e32 v12, v8
	v_mul_f32_e32 v12, v0, v12
	v_mul_f32_e32 v13, v0, v13
	v_cvt_f32_ubyte1_e32 v11, v6
	v_cvt_f32_ubyte0_e32 v10, v6
	v_cvt_pk_f16_f32 v20, v12, v13
	v_cvt_f32_ubyte3_e32 v13, v6
	v_cvt_f32_ubyte2_e32 v12, v6
	v_mul_f32_e32 v10, v0, v10
	v_mul_f32_e32 v11, v0, v11
	v_mul_f32_e32 v12, v0, v12
	v_mul_f32_e32 v13, v0, v13
	v_cvt_pk_f16_f32 v10, v10, v11
	v_cvt_pk_f16_f32 v11, v12, v13
	v_cvt_f32_ubyte3_e32 v13, v8
	v_cvt_f32_ubyte2_e32 v12, v8
	v_cvt_f32_ubyte1_e32 v15, v9
	v_cvt_f32_ubyte0_e32 v14, v9
	v_mul_f32_e32 v12, v0, v12
	v_mul_f32_e32 v13, v0, v13
	v_mul_f32_e32 v14, v0, v14
	v_mul_f32_e32 v15, v0, v15
	v_cvt_pk_f16_f32 v21, v12, v13
	v_cvt_f32_ubyte1_e32 v13, v7
	v_cvt_f32_ubyte0_e32 v12, v7
	v_cvt_pk_f16_f32 v22, v14, v15
	v_cvt_f32_ubyte3_e32 v15, v7
	v_cvt_f32_ubyte2_e32 v14, v7
	v_mul_f32_e32 v12, v0, v12
	v_mul_f32_e32 v13, v0, v13
	v_mul_f32_e32 v6, v0, v14
	v_mul_f32_e32 v7, v0, v15
	v_cvt_pk_f16_f32 v12, v12, v13
	v_cvt_pk_f16_f32 v13, v6, v7
	v_cvt_f32_ubyte3_e32 v7, v9
	v_cvt_f32_ubyte2_e32 v6, v9
	v_mul_f32_e32 v6, v0, v6
	v_mul_f32_e32 v7, v0, v7
	s_waitcnt lgkmcnt(1)
	v_div_scale_f32 v0, s[4:5], v24, v24, s18
	v_cvt_pk_f16_f32 v23, v6, v7
	v_rcp_f32_e32 v6, v0
	v_lshlrev_b32_e32 v25, 1, v60
	v_mad_u32_u24 v7, v80, s0, v25
	ds_write_b128 v7, v[10:13] offset:17408
	ds_write_b128 v7, v[20:23] offset:17424
	v_fma_f32 v7, -v0, v6, 1.0
	v_fmac_f32_e32 v6, v7, v6
	v_div_scale_f32 v7, vcc, s18, v24, s18
	v_mul_f32_e32 v8, v7, v6
	v_fma_f32 v9, -v0, v8, v7
	v_fmac_f32_e32 v8, v9, v6
	v_fma_f32 v0, -v0, v8, v7
	v_div_fmas_f32 v0, v0, v6, v8
	v_div_fixup_f32 v0, v0, v24, s18
	s_waitcnt vmcnt(8)
	v_cvt_f32_ubyte1_e32 v9, v4
	v_cvt_f32_ubyte0_e32 v8, v4
	v_mul_f32_e32 v8, v0, v8
	v_mul_f32_e32 v9, v0, v9
	v_cvt_f32_ubyte1_e32 v7, v2
	v_cvt_f32_ubyte0_e32 v6, v2
	v_cvt_pk_f16_f32 v10, v8, v9
	v_cvt_f32_ubyte3_e32 v9, v2
	v_cvt_f32_ubyte2_e32 v8, v2
	v_mul_f32_e32 v6, v0, v6
	v_mul_f32_e32 v7, v0, v7
	v_mul_f32_e32 v8, v0, v8
	v_mul_f32_e32 v9, v0, v9
	v_cvt_pk_f16_f32 v6, v6, v7
	v_cvt_pk_f16_f32 v7, v8, v9
	v_cvt_f32_ubyte3_e32 v9, v4
	v_cvt_f32_ubyte2_e32 v8, v4
	v_mul_f32_e32 v8, v0, v8
	v_mul_f32_e32 v9, v0, v9
	v_cvt_pk_f16_f32 v11, v8, v9
	v_cvt_f32_ubyte1_e32 v9, v3
	v_cvt_f32_ubyte0_e32 v8, v3
	v_cvt_f32_ubyte3_e32 v15, v3
	v_cvt_f32_ubyte2_e32 v14, v3
	v_mul_f32_e32 v8, v0, v8
	v_mul_f32_e32 v9, v0, v9
	v_mul_f32_e32 v2, v0, v14
	v_mul_f32_e32 v3, v0, v15
	v_cvt_pk_f16_f32 v8, v8, v9
	v_cvt_f32_ubyte1_e32 v13, v5
	v_cvt_f32_ubyte0_e32 v12, v5
	v_cvt_pk_f16_f32 v9, v2, v3
	v_cvt_f32_ubyte3_e32 v3, v5
	v_cvt_f32_ubyte2_e32 v2, v5
	v_mul_f32_e32 v12, v0, v12
	v_mul_f32_e32 v13, v0, v13
	v_mul_f32_e32 v2, v0, v2
	v_mul_f32_e32 v3, v0, v3
	v_mad_u32_u24 v0, v1, s0, v25
	v_cvt_pk_f16_f32 v12, v12, v13
	v_cvt_pk_f16_f32 v13, v2, v3
	ds_write_b128 v0, v[6:9] offset:17408
	ds_write_b128 v0, v[10:13] offset:17424
	v_lshlrev_b32_e32 v0, 4, v63
	v_mad_u32_u24 v60, v65, s0, v0
	s_waitcnt lgkmcnt(0)
	s_barrier
	ds_read_b128 v[0:3], v60
	ds_read_b128 v[66:69], v60 offset:32
	s_waitcnt vmcnt(7) lgkmcnt(1)
	v_mfma_f32_32x32x16_f16 v[0:15], v[0:3], v[16:19], 0
	ds_read_b128 v[20:23], v60 offset:8704
	ds_read_b128 v[70:73], v60 offset:8736
	s_add_i32 s0, s3, 32
	s_mov_b32 s4, 0xc350
	s_waitcnt lgkmcnt(1)
	v_mfma_f32_32x32x16_f16 v[16:31], v[20:23], v[16:19], 0
	s_waitcnt vmcnt(6)
	v_mfma_f32_32x32x16_f16 v[0:15], v[66:69], v[56:59], v[0:15]
	s_waitcnt lgkmcnt(0)
	v_mfma_f32_32x32x16_f16 v[16:31], v[70:73], v[56:59], v[16:31]
	ds_read_b128 v[56:59], v60 offset:64
	ds_read_b128 v[66:69], v60 offset:96
	s_waitcnt vmcnt(5) lgkmcnt(1)
	v_mfma_f32_32x32x16_f16 v[0:15], v[56:59], v[52:55], v[0:15]
	ds_read_b128 v[56:59], v60 offset:8768
	ds_read_b128 v[70:73], v60 offset:8800
	s_waitcnt lgkmcnt(1)
	v_mfma_f32_32x32x16_f16 v[16:31], v[56:59], v[52:55], v[16:31]
	s_waitcnt vmcnt(4)
	v_mfma_f32_32x32x16_f16 v[0:15], v[66:69], v[48:51], v[0:15]
	s_waitcnt lgkmcnt(0)
	v_mfma_f32_32x32x16_f16 v[16:31], v[70:73], v[48:51], v[16:31]
	ds_read_b128 v[48:51], v60 offset:128
	ds_read_b128 v[52:55], v60 offset:160
	s_waitcnt vmcnt(3) lgkmcnt(1)
	v_mfma_f32_32x32x16_f16 v[0:15], v[48:51], v[44:47], v[0:15]
	ds_read_b128 v[48:51], v60 offset:8832
	ds_read_b128 v[56:59], v60 offset:8864
	s_waitcnt lgkmcnt(1)
	v_mfma_f32_32x32x16_f16 v[16:31], v[48:51], v[44:47], v[16:31]
	s_waitcnt vmcnt(2)
	v_mfma_f32_32x32x16_f16 v[0:15], v[52:55], v[40:43], v[0:15]
	s_waitcnt lgkmcnt(0)
	v_mfma_f32_32x32x16_f16 v[16:31], v[56:59], v[40:43], v[16:31]
	ds_read_b128 v[40:43], v60 offset:192
	ds_read_b128 v[44:47], v60 offset:224
	s_waitcnt vmcnt(1) lgkmcnt(1)
	v_mfma_f32_32x32x16_f16 v[0:15], v[40:43], v[36:39], v[0:15]
	ds_read_b128 v[40:43], v60 offset:8896
	ds_read_b128 v[48:51], v60 offset:8928
	s_waitcnt lgkmcnt(1)
	v_mfma_f32_32x32x16_f16 v[16:31], v[40:43], v[36:39], v[16:31]
	v_lshl_or_b32 v36, v64, 5, v65
	v_lshlrev_b32_e32 v37, 2, v36
	global_load_dword v37, v37, s[14:15] nt
	s_waitcnt vmcnt(1)
	v_mfma_f32_32x32x16_f16 v[0:15], v[44:47], v[32:35], v[0:15]
	v_bfrev_b32_e32 v45, 1
	s_waitcnt lgkmcnt(0)
	v_mfma_f32_32x32x16_f16 v[16:31], v[48:51], v[32:35], v[16:31]
	s_waitcnt vmcnt(0)
	s_add_i32 s5, s3, 49
	s_cmp_le_u32 s5, s4
	s_cbranch_scc1 .Lfast_sum_l2
	s_nop 7
	v_add_f32_e32 v1, v37, v1
	s_nop 1
	v_add_f32_e32 v26, v37, v0
	v_mul_u32_u24_e32 v0, 0x440, v63
	v_lshl_add_u32 v0, v36, 1, v0
	ds_read_u16 v27, v0 offset:17408
	ds_read_u16 v28, v0 offset:17680
	ds_read_u16 v29, v0 offset:17952
	ds_read_u16 v30, v0 offset:18224
	ds_read_u16 v31, v0 offset:19584
	ds_read_u16 v32, v0 offset:19856
	ds_read_u16 v33, v0 offset:20128
	ds_read_u16 v34, v0 offset:20400
	ds_read_u16 v35, v0 offset:26112
	ds_read_u16 v38, v0 offset:26384
	ds_read_u16 v39, v0 offset:26656
	ds_read_u16 v40, v0 offset:26928
	ds_read_u16 v41, v0 offset:28288
	ds_read_u16 v42, v0 offset:28560
	ds_read_u16 v43, v0 offset:28832
	ds_read_u16 v44, v0 offset:29104
	s_waitcnt lgkmcnt(14)
	v_cvt_f32_f16_e32 v27, v27
	s_waitcnt lgkmcnt(7)
	v_cvt_f32_f16_e32 v35, v35
	v_add_f32_e32 v16, v37, v16
	v_lshlrev_b32_e32 v25, 2, v63
	v_add_f32_e32 v26, v26, v27
	v_add_f32_e32 v16, v16, v35
	v_max_f32_e32 v26, 0, v26
	v_max_f32_e32 v27, 0, v16
	v_add_u32_e32 v16, s3, v25
	v_add_f32_e32 v26, 0, v26
	v_cmp_gt_i32_e32 vcc, s4, v16
	v_add_u32_e32 v35, s0, v25
	v_add_f32_e32 v17, v37, v17
	v_cndmask_b32_e32 v26, 0, v26, vcc
	v_cmp_gt_i32_e32 vcc, s4, v35
	s_waitcnt lgkmcnt(6)
	v_cvt_f32_f16_e32 v35, v38
	v_add_f32_e32 v2, v37, v2
	v_cndmask_b32_e32 v27, v45, v27, vcc
	v_add_f32_e32 v26, v26, v27
	v_cvt_f32_f16_e32 v27, v28
	v_or_b32_e32 v28, 1, v25
	v_add_f32_e32 v17, v17, v35
	v_max_f32_e32 v17, 0, v17
	v_add_f32_e32 v1, v1, v27
	v_max_f32_e32 v1, 0, v1
	v_add_u32_e32 v27, s3, v28
	v_add_f32_e32 v1, v26, v1
	v_cmp_gt_i32_e32 vcc, s4, v27
	s_waitcnt lgkmcnt(5)
	v_cvt_f32_f16_e32 v27, v39
	v_add_f32_e32 v3, v37, v3
	v_cndmask_b32_e32 v1, v26, v1, vcc
	v_add_u32_e32 v26, s0, v28
	v_add_f32_e32 v17, v17, v1
	v_cmp_gt_i32_e32 vcc, s4, v26
	v_or_b32_e32 v26, 2, v25
	v_add_f32_e32 v4, v37, v4
	v_cndmask_b32_e32 v1, v1, v17, vcc
	v_cvt_f32_f16_e32 v17, v29
	v_add_f32_e32 v8, v37, v8
	v_add_f32_e32 v2, v2, v17
	v_max_f32_e32 v2, 0, v2
	v_add_f32_e32 v17, v37, v18
	v_add_u32_e32 v18, s3, v26
	v_add_f32_e32 v2, v1, v2
	v_cmp_gt_i32_e32 vcc, s4, v18
	v_add_f32_e32 v17, v17, v27
	s_waitcnt lgkmcnt(4)
	v_cvt_f32_f16_e32 v18, v40
	v_cndmask_b32_e32 v1, v1, v2, vcc
	v_add_u32_e32 v2, s0, v26
	v_cmp_gt_i32_e32 vcc, s4, v2
	v_cvt_f32_f16_e32 v2, v30
	v_max_f32_e32 v17, 0, v17
	v_add_f32_e32 v17, v17, v1
	v_cndmask_b32_e32 v1, v1, v17, vcc
	v_or_b32_e32 v17, 3, v25
	v_add_f32_e32 v2, v3, v2
	v_add_f32_e32 v3, v37, v19
	v_max_f32_e32 v2, 0, v2
	v_add_f32_e32 v3, v3, v18
	v_add_u32_e32 v18, s3, v17
	v_add_f32_e32 v2, v1, v2
	v_cmp_gt_i32_e32 vcc, s4, v18
	v_max_f32_e32 v3, 0, v3
	v_or_b32_e32 v19, 16, v25
	v_cndmask_b32_e32 v1, v1, v2, vcc
	v_add_u32_e32 v2, s0, v17
	v_cmp_gt_i32_e32 vcc, s4, v2
	v_cvt_f32_f16_e32 v2, v31
	s_waitcnt lgkmcnt(3)
	v_cvt_f32_f16_e32 v17, v41
	v_add_f32_e32 v3, v3, v1
	v_cndmask_b32_e32 v1, v1, v3, vcc
	v_or_b32_e32 v3, 8, v25
	v_add_f32_e32 v2, v4, v2
	v_add_f32_e32 v4, v37, v20
	v_max_f32_e32 v2, 0, v2
	v_add_f32_e32 v4, v4, v17
	v_add_u32_e32 v17, s3, v3
	v_add_f32_e32 v2, v1, v2
	v_cmp_gt_i32_e32 vcc, s4, v17
	v_max_f32_e32 v4, 0, v4
	s_nop 0
	v_cndmask_b32_e32 v1, v1, v2, vcc
	v_add_u32_e32 v2, s0, v3
	v_cmp_gt_i32_e32 vcc, s4, v2
	v_cvt_f32_f16_e32 v2, v32
	v_add_f32_e32 v3, v4, v1
	v_add_f32_e32 v4, v37, v5
	s_waitcnt lgkmcnt(2)
	v_cvt_f32_f16_e32 v5, v42
	v_cndmask_b32_e32 v1, v1, v3, vcc
	v_or_b32_e32 v3, 9, v25
	v_add_f32_e32 v2, v4, v2
	v_add_f32_e32 v4, v37, v21
	v_max_f32_e32 v2, 0, v2
	v_add_f32_e32 v4, v4, v5
	v_add_u32_e32 v5, s3, v3
	v_add_f32_e32 v2, v1, v2
	v_cmp_gt_i32_e32 vcc, s4, v5
	s_waitcnt lgkmcnt(1)
	v_cvt_f32_f16_e32 v5, v43
	v_max_f32_e32 v4, 0, v4
	v_cndmask_b32_e32 v1, v1, v2, vcc
	v_add_u32_e32 v2, s0, v3
	v_cmp_gt_i32_e32 vcc, s4, v2
	v_cvt_f32_f16_e32 v2, v33
	v_add_f32_e32 v3, v4, v1
	v_add_f32_e32 v4, v37, v6
	v_cndmask_b32_e32 v1, v1, v3, vcc
	v_or_b32_e32 v3, 10, v25
	v_add_f32_e32 v2, v4, v2
	v_add_f32_e32 v4, v37, v22
	v_max_f32_e32 v2, 0, v2
	v_add_f32_e32 v4, v4, v5
	v_add_u32_e32 v5, s3, v3
	v_add_f32_e32 v2, v1, v2
	v_cmp_gt_i32_e32 vcc, s4, v5
	s_waitcnt lgkmcnt(0)
	v_cvt_f32_f16_e32 v5, v44
	v_max_f32_e32 v4, 0, v4
	v_cndmask_b32_e32 v1, v1, v2, vcc
	v_add_u32_e32 v2, s0, v3
	v_cmp_gt_i32_e32 vcc, s4, v2
	v_cvt_f32_f16_e32 v2, v34
	v_add_f32_e32 v3, v4, v1
	v_add_f32_e32 v4, v37, v7
	v_cndmask_b32_e32 v1, v1, v3, vcc
	v_or_b32_e32 v3, 11, v25
	v_add_f32_e32 v2, v4, v2
	v_add_f32_e32 v4, v37, v23
	v_max_f32_e32 v2, 0, v2
	v_add_f32_e32 v4, v4, v5
	v_add_u32_e32 v5, s3, v3
	v_add_f32_e32 v2, v1, v2
	v_cmp_gt_i32_e32 vcc, s4, v5
	v_max_f32_e32 v4, 0, v4
	s_nop 0
	v_cndmask_b32_e32 v1, v1, v2, vcc
	v_add_u32_e32 v2, s0, v3
	v_add_f32_e32 v3, v4, v1
	v_cmp_gt_i32_e32 vcc, s4, v2
	s_nop 1
	v_cndmask_b32_e32 v1, v1, v3, vcc
	ds_read_u16 v2, v0 offset:30464
	ds_read_u16 v3, v0 offset:21760
	ds_read_u16 v4, v0 offset:22032
	ds_read_u16 v5, v0 offset:22304
	ds_read_u16 v6, v0 offset:22576
	ds_read_u16 v7, v0 offset:23936
	ds_read_u16 v17, v0 offset:24208
	ds_read_u16 v18, v0 offset:24480
	ds_read_u16 v0, v0 offset:24752
	s_waitcnt lgkmcnt(7)
	v_cvt_f32_f16_e32 v3, v3
	v_cvt_f32_f16_e32 v2, v2
	v_add_f32_e32 v3, v8, v3
	v_add_f32_e32 v8, v37, v24
	v_max_f32_e32 v3, 0, v3
	v_add_f32_e32 v2, v8, v2
	v_add_u32_e32 v8, s3, v19
	v_add_f32_e32 v3, v1, v3
	v_cmp_gt_i32_e32 vcc, s4, v8
	v_max_f32_e32 v2, 0, v2
	s_waitcnt lgkmcnt(0)
	v_cvt_f32_f16_e32 v0, v0
	v_cndmask_b32_e32 v1, v1, v3, vcc
	v_add_u32_e32 v3, s0, v19
	v_cmp_gt_i32_e64 s[0:1], s4, v3
	v_cvt_f32_f16_e32 v3, v4
	v_cmp_gt_u32_e32 vcc, 32, v62
	v_add_f32_e32 v2, v2, v1
	s_and_b64 s[0:1], vcc, s[0:1]
	v_cndmask_b32_e64 v1, v1, v2, s[0:1]
	v_add_f32_e32 v2, v37, v9
	v_add_f32_e32 v2, v2, v3
	v_cvt_f32_f16_e32 v4, v5
	v_max_f32_e32 v2, 0, v2
	v_add_u32_e32 v3, 17, v16
	v_add_f32_e32 v2, v1, v2
	v_cmp_gt_i32_e64 s[0:1], s4, v3
	v_add_u32_e32 v3, 18, v16
	s_nop 0
	v_cndmask_b32_e64 v1, v1, v2, s[0:1]
	v_add_f32_e32 v2, v37, v10
	v_add_f32_e32 v2, v2, v4
	v_cvt_f32_f16_e32 v4, v6
	v_max_f32_e32 v2, 0, v2
	v_add_f32_e32 v2, v1, v2
	v_cmp_gt_i32_e64 s[0:1], s4, v3
	v_add_u32_e32 v3, 19, v16
	s_nop 0
	v_cndmask_b32_e64 v1, v1, v2, s[0:1]
	v_add_f32_e32 v2, v37, v11
	v_add_f32_e32 v2, v2, v4
	v_cvt_f32_f16_e32 v4, v7
	v_max_f32_e32 v2, 0, v2
	v_add_f32_e32 v2, v1, v2
	v_cmp_gt_i32_e64 s[0:1], s4, v3
	v_add_u32_e32 v3, 24, v16
	s_nop 0
	v_cndmask_b32_e64 v1, v1, v2, s[0:1]
	v_add_f32_e32 v2, v37, v12
	v_add_f32_e32 v2, v2, v4
	v_cvt_f32_f16_e32 v4, v17
	v_max_f32_e32 v2, 0, v2
	v_add_f32_e32 v2, v1, v2
	v_cmp_gt_i32_e64 s[0:1], s4, v3
	v_add_u32_e32 v3, 25, v16
	s_nop 0
	v_cndmask_b32_e64 v1, v1, v2, s[0:1]
	v_add_f32_e32 v2, v37, v13
	v_add_f32_e32 v2, v2, v4
	v_cvt_f32_f16_e32 v4, v18
	v_max_f32_e32 v2, 0, v2
	v_add_f32_e32 v2, v1, v2
	v_cmp_gt_i32_e64 s[0:1], s4, v3
	v_add_u32_e32 v3, 26, v16
	s_nop 0
	v_cndmask_b32_e64 v1, v1, v2, s[0:1]
	v_add_f32_e32 v2, v37, v14
	v_add_f32_e32 v2, v2, v4
	v_max_f32_e32 v2, 0, v2
	v_add_f32_e32 v2, v1, v2
	v_cmp_gt_i32_e64 s[0:1], s4, v3
	s_nop 1
	v_cndmask_b32_e64 v1, v1, v2, s[0:1]
	v_add_f32_e32 v2, v37, v15
	v_add_f32_e32 v0, v2, v0
	v_max_f32_e32 v0, 0, v0
	v_add_u32_e32 v2, 27, v16
	v_add_f32_e32 v0, v1, v0
	v_cmp_gt_i32_e64 s[0:1], s4, v2
	v_and_b32_e32 v2, 64, v61
	v_add_u32_e32 v2, 64, v2
	v_cndmask_b32_e64 v0, v1, v0, s[0:1]
.Ljoin_sum_l2:
	v_xor_b32_e32 v1, 32, v61
	v_cmp_lt_i32_e64 s[0:1], v1, v2
	s_nop 1
	v_cndmask_b32_e64 v1, v61, v1, s[0:1]
	v_lshlrev_b32_e32 v1, 2, v1
	ds_bpermute_b32 v1, v1, v0
	s_and_saveexec_b64 s[0:1], vcc
	s_cbranch_execz .LBB3_28
	s_lshl_b32 s0, s2, 7
	s_and_b32 s0, s0, 0x780
	v_or_b32_e32 v2, s0, v36
	v_lshlrev_b32_e32 v2, 2, v2
	s_waitcnt lgkmcnt(0)
	v_add_f32_e32 v0, v0, v1
	s_cmp_eq_u32 s33, 0
	s_cbranch_scc0 .Lskipat_l2
	global_atomic_add_f32 v2, v0, s[6:7]
.Lskipat_l2:
.LBB3_28:
.Lpass_end_l2:
	s_mov_b64 exec, -1
	s_cmp_eq_u32 s33, 0
	s_cbranch_scc1 .Lend_l2
	s_mov_b32 s33, 0
	s_waitcnt vmcnt(0) lgkmcnt(0)
	s_barrier
	s_mov_b64 s[0:1], s[30:31]
	s_mov_b32 s2, s32
	v_mov_b32_e32 v0, v112
	s_branch .Lrep_l2

	.amdhsa_kernel _Z8k_layer2PKhPKfPK15HIP_vector_typeIjLj4EEPKjS2_PKDF16_S2_Pf
		.amdhsa_group_segment_fixed_size 39168
		.amdhsa_private_segment_fixed_size 0
		.amdhsa_kernarg_size 64
		.amdhsa_user_sgpr_count 2
		.amdhsa_user_sgpr_dispatch_ptr 0
		.amdhsa_user_sgpr_queue_ptr 0
		.amdhsa_user_sgpr_kernarg_segment_ptr 1
		.amdhsa_user_sgpr_dispatch_id 0
		.amdhsa_user_sgpr_kernarg_preload_length 0
		.amdhsa_user_sgpr_kernarg_preload_offset 0
		.amdhsa_user_sgpr_private_segment_size 0
		.amdhsa_uses_dynamic_stack 0
		.amdhsa_enable_private_segment 0
		.amdhsa_system_sgpr_workgroup_id_x 1
		.amdhsa_system_sgpr_workgroup_id_y 0
		.amdhsa_system_sgpr_workgroup_id_z 0
		.amdhsa_system_sgpr_workgroup_info 0
		.amdhsa_system_vgpr_workitem_id 0
		.amdhsa_next_free_vgpr 120
		.amdhsa_next_free_sgpr 96
		.amdhsa_accum_offset 120
		.amdhsa_reserve_vcc 1
		.amdhsa_float_round_mode_32 0
		.amdhsa_float_round_mode_16_64 0
		.amdhsa_float_denorm_mode_32 3
		.amdhsa_float_denorm_mode_16_64 3
		.amdhsa_dx10_clamp 1
		.amdhsa_ieee_mode 1
		.amdhsa_fp16_overflow 0
		.amdhsa_tg_split 0
		.amdhsa_exception_fp_ieee_invalid_op 0
		.amdhsa_exception_fp_denorm_src 0
		.amdhsa_exception_fp_ieee_div_zero 0
		.amdhsa_exception_fp_ieee_overflow 0
		.amdhsa_exception_fp_ieee_underflow 0
		.amdhsa_exception_fp_ieee_inexact 0
		.amdhsa_exception_int_div_zero 0
	.end_amdhsa_kernel

amdhsa.kernels:
  - .agpr_count:     0
    .args:
      - .actual_access:  read_only
        .address_space:  global
        .offset:         0
        .size:           8
        .value_kind:     global_buffer
      - .actual_access:  read_only
        .address_space:  global
        .offset:         8
        .size:           8
        .value_kind:     global_buffer
      - .actual_access:  write_only
        .address_space:  global
        .offset:         16
        .size:           8
        .value_kind:     global_buffer
      - .actual_access:  write_only
        .address_space:  global
        .offset:         24
        .size:           8
        .value_kind:     global_buffer
      - .actual_access:  read_only
        .address_space:  global
        .offset:         32
        .size:           8
        .value_kind:     global_buffer
      - .actual_access:  read_only
        .address_space:  global
        .offset:         40
        .size:           8
        .value_kind:     global_buffer
      - .actual_access:  read_only
        .address_space:  global
        .offset:         48
        .size:           8
        .value_kind:     global_buffer
      - .actual_access:  read_only
        .address_space:  global
        .offset:         56
        .size:           8
        .value_kind:     global_buffer
      - .actual_access:  read_only
        .address_space:  global
        .offset:         64
        .size:           8
        .value_kind:     global_buffer
      - .actual_access:  write_only
        .address_space:  global
        .offset:         72
        .size:           8
        .value_kind:     global_buffer
      - .actual_access:  write_only
        .address_space:  global
        .offset:         80
        .size:           8
        .value_kind:     global_buffer
      - .actual_access:  write_only
        .address_space:  global
        .offset:         88
        .size:           8
        .value_kind:     global_buffer
      - .actual_access:  write_only
        .address_space:  global
        .offset:         96
        .size:           8
        .value_kind:     global_buffer
      - .actual_access:  write_only
        .address_space:  global
        .offset:         104
        .size:           8
        .value_kind:     global_buffer
      - .actual_access:  write_only
        .address_space:  global
        .offset:         112
        .size:           8
        .value_kind:     global_buffer
      - .offset:         120
        .size:           4
        .value_kind:     hidden_block_count_x
      - .offset:         124
        .size:           4
        .value_kind:     hidden_block_count_y
      - .offset:         128
        .size:           4
        .value_kind:     hidden_block_count_z
      - .offset:         132
        .size:           2
        .value_kind:     hidden_group_size_x
      - .offset:         134
        .size:           2
        .value_kind:     hidden_group_size_y
      - .offset:         136
        .size:           2
        .value_kind:     hidden_group_size_z
      - .offset:         138
        .size:           2
        .value_kind:     hidden_remainder_x
      - .offset:         140
        .size:           2
        .value_kind:     hidden_remainder_y
      - .offset:         142
        .size:           2
        .value_kind:     hidden_remainder_z
      - .offset:         160
        .size:           8
        .value_kind:     hidden_global_offset_x
      - .offset:         168
        .size:           8
        .value_kind:     hidden_global_offset_y
      - .offset:         176
        .size:           8
        .value_kind:     hidden_global_offset_z
      - .offset:         184
        .size:           2
        .value_kind:     hidden_grid_dims
    .group_segment_fixed_size: 21520
    .kernarg_segment_align: 8
    .kernarg_segment_size: 376
    .language:       OpenCL C
    .language_version:
      - 2
      - 0
    .max_flat_workgroup_size: 1024
    .name:           _Z11k_chunksortPKiS0_PjS1_PKfS3_S3_S3_S3_PDF16_S4_PfS5_S4_Ph
    .private_segment_fixed_size: 0
    .sgpr_count:     32
    .sgpr_spill_count: 0
    .symbol:         _Z11k_chunksortPKiS0_PjS1_PKfS3_S3_S3_S3_PDF16_S4_PfS5_S4_Ph.kd
    .uniform_work_group_size: 1
    .uses_dynamic_stack: false
    .vgpr_count:     38
    .vgpr_spill_count: 0
    .wavefront_size: 64
  - .agpr_count:     0
    .args:
      - .actual_access:  read_only
        .address_space:  global
        .offset:         0
        .size:           8
        .value_kind:     global_buffer
      - .actual_access:  read_only
        .address_space:  global
        .offset:         8
        .size:           8
        .value_kind:     global_buffer
      - .actual_access:  read_only
        .address_space:  global
        .offset:         16
        .size:           8
        .value_kind:     global_buffer
      - .actual_access:  write_only
        .address_space:  global
        .offset:         24
        .size:           8
        .value_kind:     global_buffer
      - .actual_access:  write_only
        .address_space:  global
        .offset:         32
        .size:           8
        .value_kind:     global_buffer
      - .actual_access:  write_only
        .address_space:  global
        .offset:         40
        .size:           8
        .value_kind:     global_buffer
      - .actual_access:  write_only
        .address_space:  global
        .offset:         48
        .size:           8
        .value_kind:     global_buffer
    .group_segment_fixed_size: 22536
    .kernarg_segment_align: 8
    .kernarg_segment_size: 56
    .language:       OpenCL C
    .language_version:
      - 2
      - 0
    .max_flat_workgroup_size: 1024
    .name:           _Z5k_csrPKjS0_PKfPjPfPDF16_P15HIP_vector_typeIjLj4EE
    .private_segment_fixed_size: 0
    .sgpr_count:     44
    .sgpr_spill_count: 0
    .symbol:         _Z5k_csrPKjS0_PKfPjPfPDF16_P15HIP_vector_typeIjLj4EE.kd
    .uniform_work_group_size: 1
    .uses_dynamic_stack: false
    .vgpr_count:     48
    .vgpr_spill_count: 0
    .wavefront_size: 64
  - .agpr_count:     0
    .args:
      - .actual_access:  read_only
        .address_space:  global
        .offset:         0
        .size:           8
        .value_kind:     global_buffer
      - .actual_access:  read_only
        .address_space:  global
        .offset:         8
        .size:           8
        .value_kind:     global_buffer
      - .actual_access:  read_only
        .address_space:  global
        .offset:         16
        .size:           8
        .value_kind:     global_buffer
      - .actual_access:  read_only
        .address_space:  global
        .offset:         24
        .size:           8
        .value_kind:     global_buffer
      - .actual_access:  read_only
        .address_space:  global
        .offset:         32
        .size:           8
        .value_kind:     global_buffer
      - .actual_access:  read_only
        .address_space:  global
        .offset:         40
        .size:           8
        .value_kind:     global_buffer
      - .actual_access:  read_only
        .address_space:  global
        .offset:         48
        .size:           8
        .value_kind:     global_buffer
      - .actual_access:  write_only
        .address_space:  global
        .offset:         56
        .size:           8
        .value_kind:     global_buffer
      - .actual_access:  write_only
        .address_space:  global
        .offset:         64
        .size:           8
        .value_kind:     global_buffer
    .group_segment_fixed_size: 36112
    .kernarg_segment_align: 8
    .kernarg_segment_size: 72
    .language:       OpenCL C
    .language_version:
      - 2
      - 0
    .max_flat_workgroup_size: 256
    .name:           _Z8k_layer1PKfPKDF16_PK15HIP_vector_typeIjLj4EEPKjS0_S2_S0_PhPf
    .private_segment_fixed_size: 0
    .sgpr_count:     30
    .sgpr_spill_count: 0
    .symbol:         _Z8k_layer1PKfPKDF16_PK15HIP_vector_typeIjLj4EEPKjS0_S2_S0_PhPf.kd
    .uniform_work_group_size: 1
    .uses_dynamic_stack: false
    .vgpr_count:     128
    .vgpr_spill_count: 0
    .wavefront_size: 64
  - .agpr_count:     0
    .args:
      - .actual_access:  read_only
        .address_space:  global
        .offset:         0
        .size:           8
        .value_kind:     global_buffer
      - .actual_access:  read_only
        .address_space:  global
        .offset:         8
        .size:           8
        .value_kind:     global_buffer
      - .actual_access:  read_only
        .address_space:  global
        .offset:         16
        .size:           8
        .value_kind:     global_buffer
      - .actual_access:  read_only
        .address_space:  global
        .offset:         24
        .size:           8
        .value_kind:     global_buffer
      - .actual_access:  read_only
        .address_space:  global
        .offset:         32
        .size:           8
        .value_kind:     global_buffer
      - .actual_access:  read_only
        .address_space:  global
        .offset:         40
        .size:           8
        .value_kind:     global_buffer
      - .actual_access:  read_only
        .address_space:  global
        .offset:         48
        .size:           8
        .value_kind:     global_buffer
      - .address_space:  global
        .offset:         56
        .size:           8
        .value_kind:     global_buffer
    .group_segment_fixed_size: 39168
    .kernarg_segment_align: 8
    .kernarg_segment_size: 64
    .language:       OpenCL C
    .language_version:
      - 2
      - 0
    .max_flat_workgroup_size: 256
    .name:           _Z8k_layer2PKhPKfPK15HIP_vector_typeIjLj4EEPKjS2_PKDF16_S2_Pf
    .private_segment_fixed_size: 0
    .sgpr_count:     27
    .sgpr_spill_count: 0
    .symbol:         _Z8k_layer2PKhPKfPK15HIP_vector_typeIjLj4EEPKjS2_PKDF16_S2_Pf.kd
    .uniform_work_group_size: 1
    .uses_dynamic_stack: false
    .vgpr_count:     120
    .vgpr_spill_count: 0
    .wavefront_size: 64
  - .agpr_count:     0
    .args:
      - .actual_access:  read_only
        .address_space:  global
        .offset:         0
        .size:           8
        .value_kind:     global_buffer
      - .actual_access:  read_only
        .address_space:  global
        .offset:         8
        .size:           8
        .value_kind:     global_buffer
      - .actual_access:  read_only
        .address_space:  global
        .offset:         16
        .size:           8
        .value_kind:     global_buffer
      - .actual_access:  read_only
        .address_space:  global
        .offset:         24
        .size:           8
        .value_kind:     global_buffer
      - .actual_access:  read_only
        .address_space:  global
        .offset:         32
        .size:           8
        .value_kind:     global_buffer
      - .actual_access:  write_only
        .address_space:  global
        .offset:         40
        .size:           8
        .value_kind:     global_buffer
    .group_segment_fixed_size: 512
    .kernarg_segment_align: 8
    .kernarg_segment_size: 48
    .language:       OpenCL C
    .language_version:
      - 2
      - 0
    .max_flat_workgroup_size: 320
    .name:           _Z7k_headsPKfS0_S0_S0_S0_Pf
    .private_segment_fixed_size: 0
    .sgpr_count:     22
    .sgpr_spill_count: 0
    .symbol:         _Z7k_headsPKfS0_S0_S0_S0_Pf.kd
    .uniform_work_group_size: 1
    .uses_dynamic_stack: false
    .vgpr_count:     56
    .vgpr_spill_count: 0
    .wavefront_size: 64
